# barrier-wait conversion: waves 1-2 of every WG convert one 32x256 slab of a layer-1 expert tile per grid barrier (wave-private LDS transpose, no workgroup barrier); MoE hooks keep rounds 6-9
# speedup vs baseline: 1.0057x; 1.0039x over previous
; #define LAS __attribute__((address_space(3)))
; __device__ __forceinline__ int lane_id_v() { int l; asm volatile("v_mbcnt_lo_u32_b32 %0, -1, 0\n\tv_mbcnt_hi_u32_b32 %0, -1, %0" : "=v"(l)); return l; }
; __global__ void __launch_bounds__(NTHR, 2) mega_fwd(Args args) {
;     extern __shared__ __attribute__((aligned(16))) unsigned char lds_raw[];
;     Frame F;
;     F.lds = (LAS unsigned char*)lds_raw; F.MISC = (volatile LAS unsigned*)(F.lds + MISC_OFF);
;     F.wave = __builtin_amdgcn_readfirstlane((int)threadIdx.x >> 6); F.lane = lane_id_v(); F.tid = F.wave * 64 + F.lane;
;     F.G = gridDim.x; { const int bx = blockIdx.x; const int vcu = (F.G % 8 == 0) ? (bx % 8) * (F.G / 8) + bx / 8 : bx; F.gw = vcu * NWAVES + F.wave; F.NGW = F.G * NWAVES; }
_ZN2mk8mega_fwdENS_4ArgsE:
	v_mbcnt_lo_u32_b32 v64, -1, 0
	v_mbcnt_hi_u32_b32 v64, -1, v64
	s_mov_b32 s101, 0
	v_mov_b32_e32 v253, 0
	s_load_dword s68, s[0:1], 0xf0
	s_mov_b64 s[92:93], s[0:1]
	s_add_u32 s0, s92, 0xf0
	s_addc_u32 s1, s93, 0
	v_readfirstlane_b32 s3, v0
	v_writelane_b32 v251, s0, 0
	s_mov_b32 s10, s2
	s_nop 0
	v_writelane_b32 v251, s1, 1
	s_waitcnt lgkmcnt(0)
	s_and_b32 s0, s68, 7
	s_cmp_lg_u32 s0, 0
	s_cbranch_scc1 .LBB0_2
	s_ashr_i32 s1, s2, 31
	s_lshr_b32 s1, s1, 29
	s_add_i32 s1, s2, s1
	s_and_b32 s4, s1, -8
	s_ashr_i32 s0, s68, 3
	s_sub_i32 s4, s2, s4
	s_mul_i32 s0, s0, s4
	s_ashr_i32 s1, s1, 3
	s_add_i32 s10, s0, s1

; __device__ __forceinline__ unsigned xb_ld(unsigned* p)              { return __hip_atomic_load(p, __ATOMIC_RELAXED, __HIP_MEMORY_SCOPE_AGENT); }
; __device__ __forceinline__ unsigned xb_add(unsigned* p, unsigned v) { return __hip_atomic_fetch_add(p, v, __ATOMIC_RELAXED, __HIP_MEMORY_SCOPE_AGENT); }
; #define XB_SPIN(cond, bar) do { unsigned _sp = 0; while (cond) { __builtin_amdgcn_s_sleep(1); \
;     if ((++_sp & 255u) == 0u) { if (xb_ld(&(bar)[XB_TMO])) break; if (_sp > XB_SPIN_CAP) { atomicAdd(&(bar)[XB_TMO], 1u); break; } } } } while (0)
; __device__ __forceinline__ void xcd_barrier(const XcdBarrier& b) {
;     asm volatile("s_waitcnt vmcnt(0)" ::: "memory");
;     __syncthreads();
;     if (threadIdx.x == 0) {
;         unsigned* bar = b.bar;
;         __builtin_amdgcn_s_waitcnt(0);
;         unsigned nloc = b.st[0], nx = b.st[1];
;         if (nloc == 0u) { xcd_barrier_complete(bar, b.x, nloc, nx); b.st[0] = nloc; b.st[1] = nx; }
;         const unsigned old = xb_add(&bar[XB_XSUB(b.x)], 1u);
;         const unsigned gen = old / nloc;
;         if (old + 1u == (gen + 1u) * nloc) {
;             __builtin_amdgcn_fence(__ATOMIC_RELEASE, "agent");
;             asm volatile("s_waitcnt vmcnt(0)" ::: "memory");
;             const unsigned og = xb_add(&bar[XB_TOP], 1u);
;             const unsigned tg = og / nx;
;             if (og + 1u == (tg + 1u) * nx) xb_add(&bar[XB_TOPGEN], 1u);
;             else XB_SPIN(xb_ld(&bar[XB_TOPGEN]) == tg, bar);
;             __builtin_amdgcn_fence(__ATOMIC_ACQUIRE, "agent");
;             xb_add(&bar[XB_XGEN(b.x)], 1u);
;             asm volatile("s_waitcnt vmcnt(0)" ::: "memory");
;         } else {
;             XB_SPIN(xb_ld(&bar[XB_XGEN(b.x)]) == gen, bar);
;             __builtin_amdgcn_fence(__ATOMIC_ACQUIRE, "agent");
;             asm volatile("s_waitcnt vmcnt(0)" ::: "memory");
;         }
;     }
;     __syncthreads();
; }
.LBB0_504:
	s_cbranch_execnz .Lbw_ret_0
	s_mov_b32 s100, 0
	s_branch .Lbw_run

; __device__ __forceinline__ unsigned xb_ld(unsigned* p)              { return __hip_atomic_load(p, __ATOMIC_RELAXED, __HIP_MEMORY_SCOPE_AGENT); }
; __device__ __forceinline__ unsigned xb_add(unsigned* p, unsigned v) { return __hip_atomic_fetch_add(p, v, __ATOMIC_RELAXED, __HIP_MEMORY_SCOPE_AGENT); }
; #define XB_SPIN(cond, bar) do { unsigned _sp = 0; while (cond) { __builtin_amdgcn_s_sleep(1); \
;     if ((++_sp & 255u) == 0u) { if (xb_ld(&(bar)[XB_TMO])) break; if (_sp > XB_SPIN_CAP) { atomicAdd(&(bar)[XB_TMO], 1u); break; } } } } while (0)
; __device__ __forceinline__ void xcd_barrier(const XcdBarrier& b) {
;     asm volatile("s_waitcnt vmcnt(0)" ::: "memory");
;     __syncthreads();
;     if (threadIdx.x == 0) {
;         unsigned* bar = b.bar;
;         __builtin_amdgcn_s_waitcnt(0);
;         unsigned nloc = b.st[0], nx = b.st[1];
;         if (nloc == 0u) { xcd_barrier_complete(bar, b.x, nloc, nx); b.st[0] = nloc; b.st[1] = nx; }
;         const unsigned old = xb_add(&bar[XB_XSUB(b.x)], 1u);
;         const unsigned gen = old / nloc;
;         if (old + 1u == (gen + 1u) * nloc) {
;             __builtin_amdgcn_fence(__ATOMIC_RELEASE, "agent");
;             asm volatile("s_waitcnt vmcnt(0)" ::: "memory");
;             const unsigned og = xb_add(&bar[XB_TOP], 1u);
;             const unsigned tg = og / nx;
;             if (og + 1u == (tg + 1u) * nx) xb_add(&bar[XB_TOPGEN], 1u);
;             else XB_SPIN(xb_ld(&bar[XB_TOPGEN]) == tg, bar);
;             __builtin_amdgcn_fence(__ATOMIC_ACQUIRE, "agent");
;             xb_add(&bar[XB_XGEN(b.x)], 1u);
;             asm volatile("s_waitcnt vmcnt(0)" ::: "memory");
;         } else {
;             XB_SPIN(xb_ld(&bar[XB_XGEN(b.x)]) == gen, bar);
;             __builtin_amdgcn_fence(__ATOMIC_ACQUIRE, "agent");
;             asm volatile("s_waitcnt vmcnt(0)" ::: "memory");
;         }
;     }
;     __syncthreads();
; }
.LBB0_634:
	s_cbranch_execnz .Lbw_ret_1
	s_mov_b32 s100, 1
	s_branch .Lbw_run

; __device__ __forceinline__ unsigned xb_ld(unsigned* p)              { return __hip_atomic_load(p, __ATOMIC_RELAXED, __HIP_MEMORY_SCOPE_AGENT); }
; __device__ __forceinline__ unsigned xb_add(unsigned* p, unsigned v) { return __hip_atomic_fetch_add(p, v, __ATOMIC_RELAXED, __HIP_MEMORY_SCOPE_AGENT); }
; #define XB_SPIN(cond, bar) do { unsigned _sp = 0; while (cond) { __builtin_amdgcn_s_sleep(1); \
;     if ((++_sp & 255u) == 0u) { if (xb_ld(&(bar)[XB_TMO])) break; if (_sp > XB_SPIN_CAP) { atomicAdd(&(bar)[XB_TMO], 1u); break; } } } } while (0)
; __device__ __forceinline__ void xcd_barrier(const XcdBarrier& b) {
;     asm volatile("s_waitcnt vmcnt(0)" ::: "memory");
;     __syncthreads();
;     if (threadIdx.x == 0) {
;         unsigned* bar = b.bar;
;         __builtin_amdgcn_s_waitcnt(0);
;         unsigned nloc = b.st[0], nx = b.st[1];
;         if (nloc == 0u) { xcd_barrier_complete(bar, b.x, nloc, nx); b.st[0] = nloc; b.st[1] = nx; }
;         const unsigned old = xb_add(&bar[XB_XSUB(b.x)], 1u);
;         const unsigned gen = old / nloc;
;         if (old + 1u == (gen + 1u) * nloc) {
;             __builtin_amdgcn_fence(__ATOMIC_RELEASE, "agent");
;             asm volatile("s_waitcnt vmcnt(0)" ::: "memory");
;             const unsigned og = xb_add(&bar[XB_TOP], 1u);
;             const unsigned tg = og / nx;
;             if (og + 1u == (tg + 1u) * nx) xb_add(&bar[XB_TOPGEN], 1u);
;             else XB_SPIN(xb_ld(&bar[XB_TOPGEN]) == tg, bar);
;             __builtin_amdgcn_fence(__ATOMIC_ACQUIRE, "agent");
;             xb_add(&bar[XB_XGEN(b.x)], 1u);
;             asm volatile("s_waitcnt vmcnt(0)" ::: "memory");
;         } else {
;             XB_SPIN(xb_ld(&bar[XB_XGEN(b.x)]) == gen, bar);
;             __builtin_amdgcn_fence(__ATOMIC_ACQUIRE, "agent");
;             asm volatile("s_waitcnt vmcnt(0)" ::: "memory");
;         }
;     }
;     __syncthreads();
; }
.LBB0_770:
	s_cbranch_execnz .Lbw_ret_2
	s_mov_b32 s100, 2
	s_branch .Lbw_run

; #define LAS __attribute__((address_space(3)))
; __device__ __forceinline__ int lane_id_v() { int l; asm volatile("v_mbcnt_lo_u32_b32 %0, -1, 0\n\tv_mbcnt_hi_u32_b32 %0, -1, %0" : "=v"(l)); return l; }
; __device__ __forceinline__ void wg_convert_tile(Frame& F, const float* W, int ldw, bf16_t* WT, int Kd, int k0, int n0, int kind, const float* kgain) {
;     const int lane = lane_id_v(), w = F.wave;
;     LAS unsigned char* img = F.lds;
;     const float* src = W + (size_t)(k0 + 8 * w) * ldw + n0 + 4 * lane;
;     f32x4 ld[2][8];
; #pragma unroll
;     for (int j = 0; j < 8; ++j) ld[0][j] = __builtin_nontemporal_load((const f32x4*)(src + (size_t)j * ldw));
; #pragma unroll
;     for (int p = 0; p < 4; ++p) {
;         if (p < 3) {
; #pragma unroll
;             for (int j = 0; j < 8; ++j) ld[(p + 1) & 1][j] = __builtin_nontemporal_load((const f32x4*)(src + (size_t)(64 * (p + 1) + j) * ldw)); }
;         float g[8];
; #pragma unroll
;         for (int j = 0; j < 8; ++j) g[j] = kgain ? kgain[k0 + 64 * p + 8 * w + j] : 1.f;
; __device__ __forceinline__ void wg_conv_item(Frame& F, int l, int it) {
;     ...
;     const int e = it / 48, rr = it % 48, kind = rr / 16, item = rr % 16;
;     if (kind < 2) { const int kt = item / 2, nt = item % 2;
;         wg_convert_tile(F, F.in[24 + kind] + ((size_t)l * NE + e) * D * FH, FH, WSP(bf16_t, WS_W13 + l * SZ_W13) + (size_t)e * 1024 * D, D, 256 * kt, 256 * nt, kind, F.in[19] + l * D); }
;     else { const int kt = item / 8, nt = item % 8;
;         wg_convert_tile(F, F.in[26] + ((size_t)l * NE + e) * FH * D, D, WSP(bf16_t, WS_W2 + l * SZ_W2) + (size_t)e * D * FH, FH, 256 * kt, 256 * nt, -1, nullptr); }
.Lbw_run:
	v_writelane_b32 v253, s6, 40
	v_writelane_b32 v253, s7, 41
	v_writelane_b32 v253, s8, 42
	v_writelane_b32 v253, s9, 43
	v_writelane_b32 v253, s10, 44
	v_writelane_b32 v253, s11, 45
	v_writelane_b32 v253, s12, 46
	v_writelane_b32 v253, s13, 47
	v_writelane_b32 v253, s14, 48
	v_writelane_b32 v253, s15, 49
	v_writelane_b32 v253, s32, 50
	v_writelane_b32 v253, s33, 51
	v_writelane_b32 v253, s34, 52
	v_writelane_b32 v253, s35, 53
	v_writelane_b32 v253, s36, 54
	v_writelane_b32 v253, s37, 55
	v_writelane_b32 v253, s38, 56
	v_writelane_b32 v253, s39, 57
	v_readlane_b32 s6, v251, 2
	v_readlane_b32 s7, v253, 63
	v_readlane_b32 s9, v251, 3
	v_readlane_b32 s12, v251, 9
	v_readlane_b32 s13, v251, 10
	s_nop 4
	s_sub_u32 s6, s6, 1
	s_cmp_gt_u32 s6, 1
	s_cbranch_scc1 .Lbw_out
	s_cmp_ge_u32 s7, 16
	s_cbranch_scc1 .Lbw_out
	s_add_u32 s8, s7, 1
	s_nop 0
	v_writelane_b32 v253, s8, 63
	s_mov_b64 exec, -1
	s_load_dwordx2 s[14:15], s[12:13], 0xe0
	v_mbcnt_lo_u32_b32 v2, -1, 0
	v_mbcnt_hi_u32_b32 v2, -1, v2
	s_mul_i32 s7, s7, 2
	s_add_u32 s7, s7, s6
	s_lshr_b32 s8, s7, 3
	s_and_b32 s7, s7, 7
	s_lshr_b32 s9, s9, 3
	s_add_u32 s8, s8, 4
	s_lshl_b32 s8, s8, 8
	s_add_u32 s8, s8, s9
	s_sub_u32 s8, s8, 0x210
	s_mul_i32 s9, s8, 0xaaab
	s_lshr_b32 s9, s9, 21
	s_mul_i32 s10, s9, 48
	s_sub_u32 s8, s8, s10
	s_lshr_b32 s10, s8, 4
	s_and_b32 s8, s8, 15
	s_add_u32 s11, s9, 32
	s_lshl_b32 s11, s11, 22
	v_lshlrev_b32_e32 v3, 4, v2
	v_and_b32_e32 v10, 31, v2
	v_lshlrev_b32_e32 v10, 2, v10
	s_cmp_eq_u32 s10, 2
	s_cbranch_scc1 .Lbw_k2
	s_lshl_b32 s32, s10, 3
	s_addk_i32 s32, 0xc0
	s_load_dwordx2 s[34:35], s[12:13], s32 offset:0x0
	s_load_dwordx2 s[36:37], s[12:13], 0x98
	s_lshr_b32 s33, s8, 1
	s_and_b32 s8, s8, 1
	s_lshl_b32 s38, s33, 19
	s_add_u32 s11, s11, s38
	s_lshl_b32 s38, s8, 10
	s_add_u32 s11, s11, s38
	s_lshl_b32 s38, s7, 16
	s_add_u32 s11, s11, s38
	s_movk_i32 s32, 0x800
	s_lshl_b32 s38, s9, 22
	s_add_u32 s38, s38, 0x10500000
	s_lshl_b32 s39, s8, 21
	s_add_u32 s38, s38, s39
	s_lshl_b32 s39, s10, 19
	s_add_u32 s38, s38, s39
	s_lshl_b32 s39, s33, 9
	s_add_u32 s38, s38, s39
	s_lshl_b32 s39, s7, 6
	s_add_u32 s38, s38, s39
	s_lshl_b32 s39, s33, 10
	s_lshl_b32 s33, s7, 7
	s_add_u32 s39, s39, s33
	s_addk_i32 s39, 0x2000
	s_movk_i32 s33, 0x1000
	s_mov_b32 s10, 1
	s_waitcnt lgkmcnt(0)
	s_add_u32 s36, s36, s39
	s_addc_u32 s37, s37, 0
	global_load_dword v9, v10, s[36:37]
	s_branch .Lbw_go
.Lbw_k2:
	s_load_dwordx2 s[34:35], s[12:13], 0xd0
	s_lshr_b32 s33, s8, 3
	s_and_b32 s8, s8, 7
	s_lshl_b32 s38, s33, 21
	s_add_u32 s11, s11, s38
	s_lshl_b32 s38, s8, 10
	s_add_u32 s11, s11, s38
	s_lshl_b32 s38, s7, 18
	s_add_u32 s11, s11, s38
	s_movk_i32 s32, 0x2000
	s_lshl_b32 s38, s9, 21
	s_add_u32 s38, s38, 0x1c500000
	s_lshl_b32 s39, s8, 18
	s_add_u32 s38, s38, s39
	s_lshl_b32 s39, s33, 9
	s_add_u32 s38, s38, s39
	s_lshl_b32 s39, s7, 6
	s_add_u32 s38, s38, s39
	s_movk_i32 s33, 0x400
	s_mov_b32 s10, 0
	s_waitcnt lgkmcnt(0)
	global_load_dword v9, v10, s[34:35]
.Lbw_go:
	s_add_u32 s6, s6, 1
	s_lshl_b32 s6, s6, 14
	v_lshl_add_u32 v5, v2, 8, s6
	v_and_b32_e32 v6, 15, v2
	v_lshrrev_b32_e32 v7, 4, v2
	v_xor_b32_e32 v18, v7, v6
	v_lshl_add_u32 v17, v7, 8, s6
	v_lshrrev_b32_e32 v8, 2, v2
	v_mul_lo_u32 v8, v8, s33
	v_and_b32_e32 v11, 3, v2
	v_lshl_add_u32 v8, v11, 4, v8
	s_add_u32 s34, s34, s11
	s_addc_u32 s35, s35, 0
	s_add_u32 s14, s14, s38
	s_addc_u32 s15, s15, 0
	global_load_dwordx4 v[96:99], v3, s[34:35] sc0 sc1 nt
	s_add_u32 s34, s34, s32
	s_addc_u32 s35, s35, 0
	global_load_dwordx4 v[100:103], v3, s[34:35] sc0 sc1 nt
	s_add_u32 s34, s34, s32
	s_addc_u32 s35, s35, 0
	global_load_dwordx4 v[104:107], v3, s[34:35] sc0 sc1 nt
	s_add_u32 s34, s34, s32
	s_addc_u32 s35, s35, 0
	global_load_dwordx4 v[108:111], v3, s[34:35] sc0 sc1 nt
	s_add_u32 s34, s34, s32
	s_addc_u32 s35, s35, 0
	global_load_dwordx4 v[112:115], v3, s[34:35] sc0 sc1 nt
	s_add_u32 s34, s34, s32
	s_addc_u32 s35, s35, 0
	global_load_dwordx4 v[116:119], v3, s[34:35] sc0 sc1 nt
	s_add_u32 s34, s34, s32
	s_addc_u32 s35, s35, 0
	global_load_dwordx4 v[120:123], v3, s[34:35] sc0 sc1 nt
	s_add_u32 s34, s34, s32
	s_addc_u32 s35, s35, 0
	global_load_dwordx4 v[124:127], v3, s[34:35] sc0 sc1 nt
	s_add_u32 s34, s34, s32
	s_addc_u32 s35, s35, 0
	global_load_dwordx4 v[128:131], v3, s[34:35] sc0 sc1 nt
	s_add_u32 s34, s34, s32
	s_addc_u32 s35, s35, 0
	global_load_dwordx4 v[132:135], v3, s[34:35] sc0 sc1 nt
	s_add_u32 s34, s34, s32
	s_addc_u32 s35, s35, 0
	global_load_dwordx4 v[136:139], v3, s[34:35] sc0 sc1 nt
	s_add_u32 s34, s34, s32
	s_addc_u32 s35, s35, 0
	global_load_dwordx4 v[140:143], v3, s[34:35] sc0 sc1 nt
	s_add_u32 s34, s34, s32
	s_addc_u32 s35, s35, 0
	global_load_dwordx4 v[144:147], v3, s[34:35] sc0 sc1 nt
	s_add_u32 s34, s34, s32
	s_addc_u32 s35, s35, 0
	global_load_dwordx4 v[148:151], v3, s[34:35] sc0 sc1 nt
	s_add_u32 s34, s34, s32
	s_addc_u32 s35, s35, 0
	global_load_dwordx4 v[152:155], v3, s[34:35] sc0 sc1 nt
	s_add_u32 s34, s34, s32
	s_addc_u32 s35, s35, 0
	global_load_dwordx4 v[156:159], v3, s[34:35] sc0 sc1 nt
	s_add_u32 s34, s34, s32
	s_addc_u32 s35, s35, 0
	global_load_dwordx4 v[160:163], v3, s[34:35] sc0 sc1 nt
	s_add_u32 s34, s34, s32
	s_addc_u32 s35, s35, 0
	global_load_dwordx4 v[164:167], v3, s[34:35] sc0 sc1 nt
	s_add_u32 s34, s34, s32
	s_addc_u32 s35, s35, 0
	global_load_dwordx4 v[168:171], v3, s[34:35] sc0 sc1 nt
	s_add_u32 s34, s34, s32
	s_addc_u32 s35, s35, 0
	global_load_dwordx4 v[172:175], v3, s[34:35] sc0 sc1 nt
	s_add_u32 s34, s34, s32
	s_addc_u32 s35, s35, 0
	global_load_dwordx4 v[176:179], v3, s[34:35] sc0 sc1 nt
	s_add_u32 s34, s34, s32
	s_addc_u32 s35, s35, 0
	global_load_dwordx4 v[180:183], v3, s[34:35] sc0 sc1 nt
	s_add_u32 s34, s34, s32
	s_addc_u32 s35, s35, 0
	global_load_dwordx4 v[184:187], v3, s[34:35] sc0 sc1 nt
	s_add_u32 s34, s34, s32
	s_addc_u32 s35, s35, 0
	global_load_dwordx4 v[188:191], v3, s[34:35] sc0 sc1 nt
	s_add_u32 s34, s34, s32
	s_addc_u32 s35, s35, 0
	global_load_dwordx4 v[192:195], v3, s[34:35] sc0 sc1 nt
	s_add_u32 s34, s34, s32
	s_addc_u32 s35, s35, 0
	global_load_dwordx4 v[196:199], v3, s[34:35] sc0 sc1 nt
	s_add_u32 s34, s34, s32
	s_addc_u32 s35, s35, 0
	global_load_dwordx4 v[200:203], v3, s[34:35] sc0 sc1 nt
	s_add_u32 s34, s34, s32
	s_addc_u32 s35, s35, 0
	global_load_dwordx4 v[204:207], v3, s[34:35] sc0 sc1 nt
	s_add_u32 s34, s34, s32
	s_addc_u32 s35, s35, 0
	global_load_dwordx4 v[208:211], v3, s[34:35] sc0 sc1 nt
	s_add_u32 s34, s34, s32
	s_addc_u32 s35, s35, 0
	global_load_dwordx4 v[212:215], v3, s[34:35] sc0 sc1 nt
	s_add_u32 s34, s34, s32
	s_addc_u32 s35, s35, 0
	global_load_dwordx4 v[20:23], v3, s[34:35] sc0 sc1 nt
	s_add_u32 s34, s34, s32
	s_addc_u32 s35, s35, 0
	global_load_dwordx4 v[24:27], v3, s[34:35] sc0 sc1 nt
	s_waitcnt vmcnt(24)
	s_cmp_eq_u32 s10, 0
	s_cbranch_scc1 .Lbw_ng0
; #define LAS __attribute__((address_space(3)))
; #define SB() __builtin_amdgcn_sched_barrier(0)
; __device__ __forceinline__ unsigned cvt_pk_bf16(float lo, float hi) { unsigned r; asm volatile("v_cvt_pk_bf16_f32 %0, %1, %2" : "=v"(r) : "v"(lo), "v"(hi)); return r; }
; __device__ __forceinline__ void wg_convert_tile(Frame& F, const float* W, int ldw, bf16_t* WT, int Kd, int k0, int n0, int kind, const float* kgain) {
;     ...
;         float g[8];
; #pragma unroll
;         for (int j = 0; j < 8; ++j) g[j] = kgain ? kgain[k0 + 64 * p + 8 * w + j] : 1.f;
;         SB();
;         const unsigned kc = (unsigned)(8 * p + w);
; #pragma unroll
;         for (int c = 0; c < 4; ++c) { const int n = 4 * lane + c;
;             u32x4 o; o.x = cvt_pk_bf16(ld[p & 1][0][c] * g[0], ld[p & 1][1][c] * g[1]); o.y = cvt_pk_bf16(ld[p & 1][2][c] * g[2], ld[p & 1][3][c] * g[3]);
;                      o.z = cvt_pk_bf16(ld[p & 1][4][c] * g[4], ld[p & 1][5][c] * g[5]); o.w = cvt_pk_bf16(ld[p & 1][6][c] * g[6], ld[p & 1][7][c] * g[7]);
;             *(LAS u32x4*)(img + n * 512 + ((kc ^ (unsigned)(lane & 31)) << 4)) = o; }
	v_readlane_b32 s36, v9, 0
	v_readlane_b32 s37, v9, 1
	v_readlane_b32 s38, v9, 2
	v_readlane_b32 s39, v9, 3
	s_nop 1
	v_mul_f32_e32 v96, s36, v96
	v_mul_f32_e32 v97, s36, v97
	v_mul_f32_e32 v98, s36, v98
	v_mul_f32_e32 v99, s36, v99
	v_mul_f32_e32 v100, s37, v100
	v_mul_f32_e32 v101, s37, v101
	v_mul_f32_e32 v102, s37, v102
	v_mul_f32_e32 v103, s37, v103
	v_mul_f32_e32 v104, s38, v104
	v_mul_f32_e32 v105, s38, v105
	v_mul_f32_e32 v106, s38, v106
	v_mul_f32_e32 v107, s38, v107
	v_mul_f32_e32 v108, s39, v108
	v_mul_f32_e32 v109, s39, v109
	v_mul_f32_e32 v110, s39, v110
	v_mul_f32_e32 v111, s39, v111
	v_readlane_b32 s36, v9, 4
	v_readlane_b32 s37, v9, 5
	v_readlane_b32 s38, v9, 6
	v_readlane_b32 s39, v9, 7
	s_nop 1
	v_mul_f32_e32 v112, s36, v112
	v_mul_f32_e32 v113, s36, v113
	v_mul_f32_e32 v114, s36, v114
	v_mul_f32_e32 v115, s36, v115
	v_mul_f32_e32 v116, s37, v116
	v_mul_f32_e32 v117, s37, v117
	v_mul_f32_e32 v118, s37, v118
	v_mul_f32_e32 v119, s37, v119
	v_mul_f32_e32 v120, s38, v120
	v_mul_f32_e32 v121, s38, v121
	v_mul_f32_e32 v122, s38, v122
	v_mul_f32_e32 v123, s38, v123
	v_mul_f32_e32 v124, s39, v124
	v_mul_f32_e32 v125, s39, v125
	v_mul_f32_e32 v126, s39, v126
	v_mul_f32_e32 v127, s39, v127
.Lbw_ng0:
	v_cvt_pk_bf16_f32 v12, v96, v100
	v_cvt_pk_bf16_f32 v13, v104, v108
	v_cvt_pk_bf16_f32 v14, v112, v116
	v_cvt_pk_bf16_f32 v15, v120, v124
	v_xor_b32_e32 v11, 0, v6
	v_lshl_add_u32 v11, v11, 4, v5
	ds_write_b128 v11, v[12:15]
	v_cvt_pk_bf16_f32 v28, v97, v101
	v_cvt_pk_bf16_f32 v29, v105, v109
	v_cvt_pk_bf16_f32 v30, v113, v117
	v_cvt_pk_bf16_f32 v31, v121, v125
	v_xor_b32_e32 v16, 4, v6
	v_lshl_add_u32 v16, v16, 4, v5
	ds_write_b128 v16, v[28:31]
	v_cvt_pk_bf16_f32 v12, v98, v102
	v_cvt_pk_bf16_f32 v13, v106, v110
	v_cvt_pk_bf16_f32 v14, v114, v118
	v_cvt_pk_bf16_f32 v15, v122, v126
	v_xor_b32_e32 v11, 8, v6
	v_lshl_add_u32 v11, v11, 4, v5
	ds_write_b128 v11, v[12:15]
	v_cvt_pk_bf16_f32 v28, v99, v103
	v_cvt_pk_bf16_f32 v29, v107, v111
	v_cvt_pk_bf16_f32 v30, v115, v119
	v_cvt_pk_bf16_f32 v31, v123, v127
	v_xor_b32_e32 v16, 12, v6
	v_lshl_add_u32 v16, v16, 4, v5
	ds_write_b128 v16, v[28:31]
	s_waitcnt vmcnt(16)
	s_cmp_eq_u32 s10, 0
	s_cbranch_scc1 .Lbw_ng1
	v_readlane_b32 s36, v9, 8
	v_readlane_b32 s37, v9, 9
	v_readlane_b32 s38, v9, 10
	v_readlane_b32 s39, v9, 11
	s_nop 1
	v_mul_f32_e32 v128, s36, v128
	v_mul_f32_e32 v129, s36, v129
	v_mul_f32_e32 v130, s36, v130
	v_mul_f32_e32 v131, s36, v131
	v_mul_f32_e32 v132, s37, v132
	v_mul_f32_e32 v133, s37, v133
	v_mul_f32_e32 v134, s37, v134
	v_mul_f32_e32 v135, s37, v135
	v_mul_f32_e32 v136, s38, v136
	v_mul_f32_e32 v137, s38, v137
	v_mul_f32_e32 v138, s38, v138
	v_mul_f32_e32 v139, s38, v139
	v_mul_f32_e32 v140, s39, v140
	v_mul_f32_e32 v141, s39, v141
	v_mul_f32_e32 v142, s39, v142
	v_mul_f32_e32 v143, s39, v143
	v_readlane_b32 s36, v9, 12
	v_readlane_b32 s37, v9, 13
	v_readlane_b32 s38, v9, 14
	v_readlane_b32 s39, v9, 15
	s_nop 1
	v_mul_f32_e32 v144, s36, v144
	v_mul_f32_e32 v145, s36, v145
	v_mul_f32_e32 v146, s36, v146
	v_mul_f32_e32 v147, s36, v147
	v_mul_f32_e32 v148, s37, v148
	v_mul_f32_e32 v149, s37, v149
	v_mul_f32_e32 v150, s37, v150
	v_mul_f32_e32 v151, s37, v151
	v_mul_f32_e32 v152, s38, v152
	v_mul_f32_e32 v153, s38, v153
	v_mul_f32_e32 v154, s38, v154
	v_mul_f32_e32 v155, s38, v155
	v_mul_f32_e32 v156, s39, v156
	v_mul_f32_e32 v157, s39, v157
	v_mul_f32_e32 v158, s39, v158
	v_mul_f32_e32 v159, s39, v159
.Lbw_ng1:
	v_cvt_pk_bf16_f32 v12, v128, v132
	v_cvt_pk_bf16_f32 v13, v136, v140
	v_cvt_pk_bf16_f32 v14, v144, v148
	v_cvt_pk_bf16_f32 v15, v152, v156
	v_xor_b32_e32 v11, 1, v6
	v_lshl_add_u32 v11, v11, 4, v5
	ds_write_b128 v11, v[12:15]
	v_cvt_pk_bf16_f32 v28, v129, v133
	v_cvt_pk_bf16_f32 v29, v137, v141
	v_cvt_pk_bf16_f32 v30, v145, v149
	v_cvt_pk_bf16_f32 v31, v153, v157
	v_xor_b32_e32 v16, 5, v6
	v_lshl_add_u32 v16, v16, 4, v5
	ds_write_b128 v16, v[28:31]
	v_cvt_pk_bf16_f32 v12, v130, v134
	v_cvt_pk_bf16_f32 v13, v138, v142
	v_cvt_pk_bf16_f32 v14, v146, v150
	v_cvt_pk_bf16_f32 v15, v154, v158
	v_xor_b32_e32 v11, 9, v6
	v_lshl_add_u32 v11, v11, 4, v5
	ds_write_b128 v11, v[12:15]
	v_cvt_pk_bf16_f32 v28, v131, v135
	v_cvt_pk_bf16_f32 v29, v139, v143
	v_cvt_pk_bf16_f32 v30, v147, v151
	v_cvt_pk_bf16_f32 v31, v155, v159
	v_xor_b32_e32 v16, 13, v6
	v_lshl_add_u32 v16, v16, 4, v5
	ds_write_b128 v16, v[28:31]
	s_waitcnt vmcnt(8)
	s_cmp_eq_u32 s10, 0
	s_cbranch_scc1 .Lbw_ng2
	v_readlane_b32 s36, v9, 16
	v_readlane_b32 s37, v9, 17
	v_readlane_b32 s38, v9, 18
	v_readlane_b32 s39, v9, 19
	s_nop 1
	v_mul_f32_e32 v160, s36, v160
	v_mul_f32_e32 v161, s36, v161
	v_mul_f32_e32 v162, s36, v162
	v_mul_f32_e32 v163, s36, v163
	v_mul_f32_e32 v164, s37, v164
	v_mul_f32_e32 v165, s37, v165
	v_mul_f32_e32 v166, s37, v166
	v_mul_f32_e32 v167, s37, v167
	v_mul_f32_e32 v168, s38, v168
	v_mul_f32_e32 v169, s38, v169
	v_mul_f32_e32 v170, s38, v170
	v_mul_f32_e32 v171, s38, v171
	v_mul_f32_e32 v172, s39, v172
	v_mul_f32_e32 v173, s39, v173
	v_mul_f32_e32 v174, s39, v174
	v_mul_f32_e32 v175, s39, v175
	v_readlane_b32 s36, v9, 20
	v_readlane_b32 s37, v9, 21
	v_readlane_b32 s38, v9, 22
	v_readlane_b32 s39, v9, 23
	s_nop 1
	v_mul_f32_e32 v176, s36, v176
	v_mul_f32_e32 v177, s36, v177
	v_mul_f32_e32 v178, s36, v178
	v_mul_f32_e32 v179, s36, v179
	v_mul_f32_e32 v180, s37, v180
	v_mul_f32_e32 v181, s37, v181
	v_mul_f32_e32 v182, s37, v182
	v_mul_f32_e32 v183, s37, v183
	v_mul_f32_e32 v184, s38, v184
	v_mul_f32_e32 v185, s38, v185
	v_mul_f32_e32 v186, s38, v186
	v_mul_f32_e32 v187, s38, v187
	v_mul_f32_e32 v188, s39, v188
	v_mul_f32_e32 v189, s39, v189
	v_mul_f32_e32 v190, s39, v190
	v_mul_f32_e32 v191, s39, v191
; #define LAS __attribute__((address_space(3)))
; #define SB() __builtin_amdgcn_sched_barrier(0)
; __device__ __forceinline__ unsigned cvt_pk_bf16(float lo, float hi) { unsigned r; asm volatile("v_cvt_pk_bf16_f32 %0, %1, %2" : "=v"(r) : "v"(lo), "v"(hi)); return r; }
; __device__ __forceinline__ void wg_convert_tile(Frame& F, const float* W, int ldw, bf16_t* WT, int Kd, int k0, int n0, int kind, const float* kgain) {
;     ...
;         float g[8];
; #pragma unroll
;         for (int j = 0; j < 8; ++j) g[j] = kgain ? kgain[k0 + 64 * p + 8 * w + j] : 1.f;
;         SB();
;         const unsigned kc = (unsigned)(8 * p + w);
; #pragma unroll
;         for (int c = 0; c < 4; ++c) { const int n = 4 * lane + c;
;             u32x4 o; o.x = cvt_pk_bf16(ld[p & 1][0][c] * g[0], ld[p & 1][1][c] * g[1]); o.y = cvt_pk_bf16(ld[p & 1][2][c] * g[2], ld[p & 1][3][c] * g[3]);
;                      o.z = cvt_pk_bf16(ld[p & 1][4][c] * g[4], ld[p & 1][5][c] * g[5]); o.w = cvt_pk_bf16(ld[p & 1][6][c] * g[6], ld[p & 1][7][c] * g[7]);
;             *(LAS u32x4*)(img + n * 512 + ((kc ^ (unsigned)(lane & 31)) << 4)) = o; }
.Lbw_ng2:
	v_cvt_pk_bf16_f32 v12, v160, v164
	v_cvt_pk_bf16_f32 v13, v168, v172
	v_cvt_pk_bf16_f32 v14, v176, v180
	v_cvt_pk_bf16_f32 v15, v184, v188
	v_xor_b32_e32 v11, 2, v6
	v_lshl_add_u32 v11, v11, 4, v5
	ds_write_b128 v11, v[12:15]
	v_cvt_pk_bf16_f32 v28, v161, v165
	v_cvt_pk_bf16_f32 v29, v169, v173
	v_cvt_pk_bf16_f32 v30, v177, v181
	v_cvt_pk_bf16_f32 v31, v185, v189
	v_xor_b32_e32 v16, 6, v6
	v_lshl_add_u32 v16, v16, 4, v5
	ds_write_b128 v16, v[28:31]
	v_cvt_pk_bf16_f32 v12, v162, v166
	v_cvt_pk_bf16_f32 v13, v170, v174
	v_cvt_pk_bf16_f32 v14, v178, v182
	v_cvt_pk_bf16_f32 v15, v186, v190
	v_xor_b32_e32 v11, 10, v6
	v_lshl_add_u32 v11, v11, 4, v5
	ds_write_b128 v11, v[12:15]
	v_cvt_pk_bf16_f32 v28, v163, v167
	v_cvt_pk_bf16_f32 v29, v171, v175
	v_cvt_pk_bf16_f32 v30, v179, v183
	v_cvt_pk_bf16_f32 v31, v187, v191
	v_xor_b32_e32 v16, 14, v6
	v_lshl_add_u32 v16, v16, 4, v5
	ds_write_b128 v16, v[28:31]
	s_waitcnt vmcnt(0)
	s_cmp_eq_u32 s10, 0
	s_cbranch_scc1 .Lbw_ng3
	v_readlane_b32 s36, v9, 24
	v_readlane_b32 s37, v9, 25
	v_readlane_b32 s38, v9, 26
	v_readlane_b32 s39, v9, 27
	s_nop 1
	v_mul_f32_e32 v192, s36, v192
	v_mul_f32_e32 v193, s36, v193
	v_mul_f32_e32 v194, s36, v194
	v_mul_f32_e32 v195, s36, v195
	v_mul_f32_e32 v196, s37, v196
	v_mul_f32_e32 v197, s37, v197
	v_mul_f32_e32 v198, s37, v198
	v_mul_f32_e32 v199, s37, v199
	v_mul_f32_e32 v200, s38, v200
	v_mul_f32_e32 v201, s38, v201
	v_mul_f32_e32 v202, s38, v202
	v_mul_f32_e32 v203, s38, v203
	v_mul_f32_e32 v204, s39, v204
	v_mul_f32_e32 v205, s39, v205
	v_mul_f32_e32 v206, s39, v206
	v_mul_f32_e32 v207, s39, v207
	v_readlane_b32 s36, v9, 28
	v_readlane_b32 s37, v9, 29
	v_readlane_b32 s38, v9, 30
	v_readlane_b32 s39, v9, 31
	s_nop 1
	v_mul_f32_e32 v208, s36, v208
	v_mul_f32_e32 v209, s36, v209
	v_mul_f32_e32 v210, s36, v210
	v_mul_f32_e32 v211, s36, v211
	v_mul_f32_e32 v212, s37, v212
	v_mul_f32_e32 v213, s37, v213
	v_mul_f32_e32 v214, s37, v214
	v_mul_f32_e32 v215, s37, v215
	v_mul_f32_e32 v20, s38, v20
	v_mul_f32_e32 v21, s38, v21
	v_mul_f32_e32 v22, s38, v22
	v_mul_f32_e32 v23, s38, v23
	v_mul_f32_e32 v24, s39, v24
	v_mul_f32_e32 v25, s39, v25
	v_mul_f32_e32 v26, s39, v26
	v_mul_f32_e32 v27, s39, v27
; #define LAS __attribute__((address_space(3)))
; #define GAS __attribute__((address_space(1)))
; #define SB() __builtin_amdgcn_sched_barrier(0)
; #define LDS_WAIT() asm volatile("s_waitcnt lgkmcnt(0)" ::: "memory")
; __device__ __forceinline__ void wg_convert_tile(Frame& F, const float* W, int ldw, bf16_t* WT, int Kd, int k0, int n0, int kind, const float* kgain) {
;     ...
; #pragma unroll
;     for (int t = 0; t < 16; t += 4) { u32x4 v[4];
; #pragma unroll
;         for (int q = 0; q < 4; ++q) { const int idx = (t + q) * 512 + w * 64 + lane, n = idx >> 5, kc = idx & 31; v[q] = *(const LAS u32x4*)(img + n * 512 + ((kc ^ ((n >> 2) & 31)) << 4)); }
;         SB();
; #pragma unroll
;         for (int q = 0; q < 4; ++q) { const int idx = (t + q) * 512 + w * 64 + lane, n = idx >> 5, kc = idx & 31, nn = n0 + n;
;             const int row = kind < 0 ? nn : ((nn >> 7) * 256 + kind * 128 + (nn & 127));
;             __builtin_nontemporal_store(v[q], (GAS u32x4*)(WT + (size_t)row * Kd + k0 + 8 * kc)); }
;         SB(); }
;     LDS_WAIT(); __syncthreads();
.Lbw_ng3:
	v_cvt_pk_bf16_f32 v12, v192, v196
	v_cvt_pk_bf16_f32 v13, v200, v204
	v_cvt_pk_bf16_f32 v14, v208, v212
	v_cvt_pk_bf16_f32 v15, v20, v24
	v_xor_b32_e32 v11, 3, v6
	v_lshl_add_u32 v11, v11, 4, v5
	ds_write_b128 v11, v[12:15]
	v_cvt_pk_bf16_f32 v28, v193, v197
	v_cvt_pk_bf16_f32 v29, v201, v205
	v_cvt_pk_bf16_f32 v30, v209, v213
	v_cvt_pk_bf16_f32 v31, v21, v25
	v_xor_b32_e32 v16, 7, v6
	v_lshl_add_u32 v16, v16, 4, v5
	ds_write_b128 v16, v[28:31]
	v_cvt_pk_bf16_f32 v12, v194, v198
	v_cvt_pk_bf16_f32 v13, v202, v206
	v_cvt_pk_bf16_f32 v14, v210, v214
	v_cvt_pk_bf16_f32 v15, v22, v26
	v_xor_b32_e32 v11, 11, v6
	v_lshl_add_u32 v11, v11, 4, v5
	ds_write_b128 v11, v[12:15]
	v_cvt_pk_bf16_f32 v28, v195, v199
	v_cvt_pk_bf16_f32 v29, v203, v207
	v_cvt_pk_bf16_f32 v30, v211, v215
	v_cvt_pk_bf16_f32 v31, v23, v27
	v_xor_b32_e32 v16, 15, v6
	v_lshl_add_u32 v16, v16, 4, v5
	ds_write_b128 v16, v[28:31]
	s_waitcnt lgkmcnt(0)
	v_xor_b32_e32 v11, 0, v18
	v_lshl_add_u32 v11, v11, 4, v17
	ds_read_b128 v[96:99], v11
	v_xor_b32_e32 v16, 4, v18
	v_lshl_add_u32 v16, v16, 4, v17
	ds_read_b128 v[100:103], v16 offset:1024
	v_xor_b32_e32 v11, 8, v18
	v_lshl_add_u32 v11, v11, 4, v17
	ds_read_b128 v[104:107], v11 offset:2048
	v_xor_b32_e32 v16, 12, v18
	v_lshl_add_u32 v16, v16, 4, v17
	ds_read_b128 v[108:111], v16 offset:3072
	s_waitcnt lgkmcnt(0)
	s_movk_i32 s36, 0
	s_mul_i32 s36, s36, s33
	s_add_u32 s38, s14, s36
	s_addc_u32 s39, s15, 0
	global_store_dwordx4 v8, v[96:99], s[38:39]
	s_movk_i32 s36, 16
	s_mul_i32 s36, s36, s33
	s_add_u32 s38, s14, s36
	s_addc_u32 s39, s15, 0
	global_store_dwordx4 v8, v[100:103], s[38:39]
	s_movk_i32 s36, 32
	s_mul_i32 s36, s36, s33
	s_add_u32 s38, s14, s36
	s_addc_u32 s39, s15, 0
	global_store_dwordx4 v8, v[104:107], s[38:39]
	s_movk_i32 s36, 48
	s_mul_i32 s36, s36, s33
	s_add_u32 s38, s14, s36
	s_addc_u32 s39, s15, 0
	global_store_dwordx4 v8, v[108:111], s[38:39]
	v_xor_b32_e32 v11, 0, v18
	v_lshl_add_u32 v11, v11, 4, v17
	ds_read_b128 v[96:99], v11 offset:4096
	v_xor_b32_e32 v16, 4, v18
	v_lshl_add_u32 v16, v16, 4, v17
	ds_read_b128 v[100:103], v16 offset:5120
	v_xor_b32_e32 v11, 8, v18
	v_lshl_add_u32 v11, v11, 4, v17
	ds_read_b128 v[104:107], v11 offset:6144
	v_xor_b32_e32 v16, 12, v18
	v_lshl_add_u32 v16, v16, 4, v17
	ds_read_b128 v[108:111], v16 offset:7168
	s_waitcnt lgkmcnt(0)
	s_movk_i32 s36, 64
	s_mul_i32 s36, s36, s33
	s_add_u32 s38, s14, s36
	s_addc_u32 s39, s15, 0
	global_store_dwordx4 v8, v[96:99], s[38:39]
	s_movk_i32 s36, 80
	s_mul_i32 s36, s36, s33
	s_add_u32 s38, s14, s36
	s_addc_u32 s39, s15, 0
	global_store_dwordx4 v8, v[100:103], s[38:39]
	s_movk_i32 s36, 96
	s_mul_i32 s36, s36, s33
	s_add_u32 s38, s14, s36
	s_addc_u32 s39, s15, 0
	global_store_dwordx4 v8, v[104:107], s[38:39]
	s_movk_i32 s36, 112
	s_mul_i32 s36, s36, s33
	s_add_u32 s38, s14, s36
	s_addc_u32 s39, s15, 0
	global_store_dwordx4 v8, v[108:111], s[38:39]
	v_xor_b32_e32 v11, 0, v18
	v_lshl_add_u32 v11, v11, 4, v17
	ds_read_b128 v[96:99], v11 offset:8192
	v_xor_b32_e32 v16, 4, v18
	v_lshl_add_u32 v16, v16, 4, v17
	ds_read_b128 v[100:103], v16 offset:9216
	v_xor_b32_e32 v11, 8, v18
	v_lshl_add_u32 v11, v11, 4, v17
	ds_read_b128 v[104:107], v11 offset:10240
	v_xor_b32_e32 v16, 12, v18
	v_lshl_add_u32 v16, v16, 4, v17
	ds_read_b128 v[108:111], v16 offset:11264
	s_waitcnt lgkmcnt(0)
	s_movk_i32 s36, 128
	s_cmp_eq_u32 s10, 1
	s_cselect_b32 s36, 256, s36
	s_mul_i32 s36, s36, s33
	s_add_u32 s38, s14, s36
	s_addc_u32 s39, s15, 0
	global_store_dwordx4 v8, v[96:99], s[38:39]
	s_movk_i32 s36, 144
	s_cmp_eq_u32 s10, 1
	s_cselect_b32 s36, 272, s36
	s_mul_i32 s36, s36, s33
	s_add_u32 s38, s14, s36
	s_addc_u32 s39, s15, 0
	global_store_dwordx4 v8, v[100:103], s[38:39]
	s_movk_i32 s36, 160
	s_cmp_eq_u32 s10, 1
	s_cselect_b32 s36, 288, s36
	s_mul_i32 s36, s36, s33
	s_add_u32 s38, s14, s36
	s_addc_u32 s39, s15, 0
	global_store_dwordx4 v8, v[104:107], s[38:39]
	s_movk_i32 s36, 176
	s_cmp_eq_u32 s10, 1
	s_cselect_b32 s36, 304, s36
	s_mul_i32 s36, s36, s33
	s_add_u32 s38, s14, s36
	s_addc_u32 s39, s15, 0
	global_store_dwordx4 v8, v[108:111], s[38:39]
	v_xor_b32_e32 v11, 0, v18
	v_lshl_add_u32 v11, v11, 4, v17
	ds_read_b128 v[96:99], v11 offset:12288
	v_xor_b32_e32 v16, 4, v18
	v_lshl_add_u32 v16, v16, 4, v17
	ds_read_b128 v[100:103], v16 offset:13312
	v_xor_b32_e32 v11, 8, v18
	v_lshl_add_u32 v11, v11, 4, v17
	ds_read_b128 v[104:107], v11 offset:14336
	v_xor_b32_e32 v16, 12, v18
	v_lshl_add_u32 v16, v16, 4, v17
	ds_read_b128 v[108:111], v16 offset:15360
	s_waitcnt lgkmcnt(0)
	s_movk_i32 s36, 192
	s_cmp_eq_u32 s10, 1
	s_cselect_b32 s36, 320, s36
	s_mul_i32 s36, s36, s33
	s_add_u32 s38, s14, s36
	s_addc_u32 s39, s15, 0
	global_store_dwordx4 v8, v[96:99], s[38:39]
	s_movk_i32 s36, 208
	s_cmp_eq_u32 s10, 1
	s_cselect_b32 s36, 336, s36
	s_mul_i32 s36, s36, s33
	s_add_u32 s38, s14, s36
	s_addc_u32 s39, s15, 0
	global_store_dwordx4 v8, v[100:103], s[38:39]
	s_movk_i32 s36, 224
	s_cmp_eq_u32 s10, 1
	s_cselect_b32 s36, 352, s36
	s_mul_i32 s36, s36, s33
	s_add_u32 s38, s14, s36
	s_addc_u32 s39, s15, 0
	global_store_dwordx4 v8, v[104:107], s[38:39]
	s_movk_i32 s36, 240
	s_cmp_eq_u32 s10, 1
	s_cselect_b32 s36, 368, s36
	s_mul_i32 s36, s36, s33
	s_add_u32 s38, s14, s36
	s_addc_u32 s39, s15, 0
	global_store_dwordx4 v8, v[108:111], s[38:39]
	s_mov_b64 exec, 0
.Lbw_out:
	v_readlane_b32 s6, v253, 40
	v_readlane_b32 s7, v253, 41
	v_readlane_b32 s8, v253, 42
	v_readlane_b32 s9, v253, 43
	v_readlane_b32 s10, v253, 44
	v_readlane_b32 s11, v253, 45
	v_readlane_b32 s12, v253, 46
	v_readlane_b32 s13, v253, 47
	v_readlane_b32 s14, v253, 48
	v_readlane_b32 s15, v253, 49
	v_readlane_b32 s32, v253, 50
	v_readlane_b32 s33, v253, 51
	v_readlane_b32 s34, v253, 52
	v_readlane_b32 s35, v253, 53
	v_readlane_b32 s36, v253, 54
	v_readlane_b32 s37, v253, 55
	v_readlane_b32 s38, v253, 56
	v_readlane_b32 s39, v253, 57
	s_nop 7
	s_cmp_eq_u32 s100, 0
	s_cbranch_scc1 .Lbw_ret_0
	s_cmp_eq_u32 s100, 1
	s_cbranch_scc1 .Lbw_ret_1
	s_cmp_eq_u32 s100, 2
	s_cbranch_scc1 .Lbw_ret_2
	s_cmp_eq_u32 s100, 3
	s_cbranch_scc1 .Lbw_ret_3
	s_cmp_eq_u32 s100, 4
	s_cbranch_scc1 .Lbw_ret_4
	s_cmp_eq_u32 s100, 5
	s_cbranch_scc1 .Lbw_ret_5
	s_cmp_eq_u32 s100, 6
	s_cbranch_scc1 .Lbw_ret_6
	s_cmp_eq_u32 s100, 7
	s_cbranch_scc1 .Lbw_ret_7
	s_branch .Lbw_ret_8

; __device__ __forceinline__ unsigned xb_ld(unsigned* p)              { return __hip_atomic_load(p, __ATOMIC_RELAXED, __HIP_MEMORY_SCOPE_AGENT); }
; __device__ __forceinline__ unsigned xb_add(unsigned* p, unsigned v) { return __hip_atomic_fetch_add(p, v, __ATOMIC_RELAXED, __HIP_MEMORY_SCOPE_AGENT); }
; #define XB_SPIN(cond, bar) do { unsigned _sp = 0; while (cond) { __builtin_amdgcn_s_sleep(1); \
;     if ((++_sp & 255u) == 0u) { if (xb_ld(&(bar)[XB_TMO])) break; if (_sp > XB_SPIN_CAP) { atomicAdd(&(bar)[XB_TMO], 1u); break; } } } } while (0)
; __device__ __forceinline__ void xcd_barrier(const XcdBarrier& b) {
;     asm volatile("s_waitcnt vmcnt(0)" ::: "memory");
;     __syncthreads();
;     if (threadIdx.x == 0) {
;         unsigned* bar = b.bar;
;         __builtin_amdgcn_s_waitcnt(0);
;         unsigned nloc = b.st[0], nx = b.st[1];
;         if (nloc == 0u) { xcd_barrier_complete(bar, b.x, nloc, nx); b.st[0] = nloc; b.st[1] = nx; }
;         const unsigned old = xb_add(&bar[XB_XSUB(b.x)], 1u);
;         const unsigned gen = old / nloc;
;         if (old + 1u == (gen + 1u) * nloc) {
;             __builtin_amdgcn_fence(__ATOMIC_RELEASE, "agent");
;             asm volatile("s_waitcnt vmcnt(0)" ::: "memory");
;             const unsigned og = xb_add(&bar[XB_TOP], 1u);
;             const unsigned tg = og / nx;
;             if (og + 1u == (tg + 1u) * nx) xb_add(&bar[XB_TOPGEN], 1u);
;             else XB_SPIN(xb_ld(&bar[XB_TOPGEN]) == tg, bar);
;             __builtin_amdgcn_fence(__ATOMIC_ACQUIRE, "agent");
;             xb_add(&bar[XB_XGEN(b.x)], 1u);
;             asm volatile("s_waitcnt vmcnt(0)" ::: "memory");
;         } else {
;             XB_SPIN(xb_ld(&bar[XB_XGEN(b.x)]) == gen, bar);
;             __builtin_amdgcn_fence(__ATOMIC_ACQUIRE, "agent");
;             asm volatile("s_waitcnt vmcnt(0)" ::: "memory");
;         }
;     }
;     __syncthreads();
; }
.LBB0_1057:
	s_cbranch_execnz .Lbw_ret_3
	s_mov_b32 s100, 3
	s_branch .Lbw_run

; __device__ __forceinline__ unsigned xb_ld(unsigned* p)              { return __hip_atomic_load(p, __ATOMIC_RELAXED, __HIP_MEMORY_SCOPE_AGENT); }
; __device__ __forceinline__ unsigned xb_add(unsigned* p, unsigned v) { return __hip_atomic_fetch_add(p, v, __ATOMIC_RELAXED, __HIP_MEMORY_SCOPE_AGENT); }
; #define XB_SPIN(cond, bar) do { unsigned _sp = 0; while (cond) { __builtin_amdgcn_s_sleep(1); \
;     if ((++_sp & 255u) == 0u) { if (xb_ld(&(bar)[XB_TMO])) break; if (_sp > XB_SPIN_CAP) { atomicAdd(&(bar)[XB_TMO], 1u); break; } } } } while (0)
; __device__ __forceinline__ void xcd_barrier(const XcdBarrier& b) {
;     asm volatile("s_waitcnt vmcnt(0)" ::: "memory");
;     __syncthreads();
;     if (threadIdx.x == 0) {
;         unsigned* bar = b.bar;
;         __builtin_amdgcn_s_waitcnt(0);
;         unsigned nloc = b.st[0], nx = b.st[1];
;         if (nloc == 0u) { xcd_barrier_complete(bar, b.x, nloc, nx); b.st[0] = nloc; b.st[1] = nx; }
;         const unsigned old = xb_add(&bar[XB_XSUB(b.x)], 1u);
;         const unsigned gen = old / nloc;
;         if (old + 1u == (gen + 1u) * nloc) {
;             __builtin_amdgcn_fence(__ATOMIC_RELEASE, "agent");
;             asm volatile("s_waitcnt vmcnt(0)" ::: "memory");
;             const unsigned og = xb_add(&bar[XB_TOP], 1u);
;             const unsigned tg = og / nx;
;             if (og + 1u == (tg + 1u) * nx) xb_add(&bar[XB_TOPGEN], 1u);
;             else XB_SPIN(xb_ld(&bar[XB_TOPGEN]) == tg, bar);
;             __builtin_amdgcn_fence(__ATOMIC_ACQUIRE, "agent");
;             xb_add(&bar[XB_XGEN(b.x)], 1u);
;             asm volatile("s_waitcnt vmcnt(0)" ::: "memory");
;         } else {
;             XB_SPIN(xb_ld(&bar[XB_XGEN(b.x)]) == gen, bar);
;             __builtin_amdgcn_fence(__ATOMIC_ACQUIRE, "agent");
;             asm volatile("s_waitcnt vmcnt(0)" ::: "memory");
;         }
;     }
;     __syncthreads();
; }
.LBB0_1177:
	s_cbranch_execnz .Lbw_ret_4
	s_mov_b32 s100, 4
	s_branch .Lbw_run

; __device__ __forceinline__ unsigned xb_ld(unsigned* p)              { return __hip_atomic_load(p, __ATOMIC_RELAXED, __HIP_MEMORY_SCOPE_AGENT); }
; __device__ __forceinline__ unsigned xb_add(unsigned* p, unsigned v) { return __hip_atomic_fetch_add(p, v, __ATOMIC_RELAXED, __HIP_MEMORY_SCOPE_AGENT); }
; #define XB_SPIN(cond, bar) do { unsigned _sp = 0; while (cond) { __builtin_amdgcn_s_sleep(1); \
;     if ((++_sp & 255u) == 0u) { if (xb_ld(&(bar)[XB_TMO])) break; if (_sp > XB_SPIN_CAP) { atomicAdd(&(bar)[XB_TMO], 1u); break; } } } } while (0)
; __device__ __forceinline__ void xcd_barrier(const XcdBarrier& b) {
;     asm volatile("s_waitcnt vmcnt(0)" ::: "memory");
;     __syncthreads();
;     if (threadIdx.x == 0) {
;         unsigned* bar = b.bar;
;         __builtin_amdgcn_s_waitcnt(0);
;         unsigned nloc = b.st[0], nx = b.st[1];
;         if (nloc == 0u) { xcd_barrier_complete(bar, b.x, nloc, nx); b.st[0] = nloc; b.st[1] = nx; }
;         const unsigned old = xb_add(&bar[XB_XSUB(b.x)], 1u);
;         const unsigned gen = old / nloc;
;         if (old + 1u == (gen + 1u) * nloc) {
;             __builtin_amdgcn_fence(__ATOMIC_RELEASE, "agent");
;             asm volatile("s_waitcnt vmcnt(0)" ::: "memory");
;             const unsigned og = xb_add(&bar[XB_TOP], 1u);
;             const unsigned tg = og / nx;
;             if (og + 1u == (tg + 1u) * nx) xb_add(&bar[XB_TOPGEN], 1u);
;             else XB_SPIN(xb_ld(&bar[XB_TOPGEN]) == tg, bar);
;             __builtin_amdgcn_fence(__ATOMIC_ACQUIRE, "agent");
;             xb_add(&bar[XB_XGEN(b.x)], 1u);
;             asm volatile("s_waitcnt vmcnt(0)" ::: "memory");
;         } else {
;             XB_SPIN(xb_ld(&bar[XB_XGEN(b.x)]) == gen, bar);
;             __builtin_amdgcn_fence(__ATOMIC_ACQUIRE, "agent");
;             asm volatile("s_waitcnt vmcnt(0)" ::: "memory");
;         }
;     }
;     __syncthreads();
; }
.LBB0_1264:
	s_cbranch_execnz .Lbw_ret_5
	s_mov_b32 s100, 5
	s_branch .Lbw_run

; __device__ __forceinline__ unsigned xb_ld(unsigned* p)              { return __hip_atomic_load(p, __ATOMIC_RELAXED, __HIP_MEMORY_SCOPE_AGENT); }
; __device__ __forceinline__ unsigned xb_add(unsigned* p, unsigned v) { return __hip_atomic_fetch_add(p, v, __ATOMIC_RELAXED, __HIP_MEMORY_SCOPE_AGENT); }
; #define XB_SPIN(cond, bar) do { unsigned _sp = 0; while (cond) { __builtin_amdgcn_s_sleep(1); \
;     if ((++_sp & 255u) == 0u) { if (xb_ld(&(bar)[XB_TMO])) break; if (_sp > XB_SPIN_CAP) { atomicAdd(&(bar)[XB_TMO], 1u); break; } } } } while (0)
; __device__ __forceinline__ void xcd_barrier(const XcdBarrier& b) {
;     asm volatile("s_waitcnt vmcnt(0)" ::: "memory");
;     __syncthreads();
;     if (threadIdx.x == 0) {
;         unsigned* bar = b.bar;
;         __builtin_amdgcn_s_waitcnt(0);
;         unsigned nloc = b.st[0], nx = b.st[1];
;         if (nloc == 0u) { xcd_barrier_complete(bar, b.x, nloc, nx); b.st[0] = nloc; b.st[1] = nx; }
;         const unsigned old = xb_add(&bar[XB_XSUB(b.x)], 1u);
;         const unsigned gen = old / nloc;
;         if (old + 1u == (gen + 1u) * nloc) {
;             __builtin_amdgcn_fence(__ATOMIC_RELEASE, "agent");
;             asm volatile("s_waitcnt vmcnt(0)" ::: "memory");
;             const unsigned og = xb_add(&bar[XB_TOP], 1u);
;             const unsigned tg = og / nx;
;             if (og + 1u == (tg + 1u) * nx) xb_add(&bar[XB_TOPGEN], 1u);
;             else XB_SPIN(xb_ld(&bar[XB_TOPGEN]) == tg, bar);
;             __builtin_amdgcn_fence(__ATOMIC_ACQUIRE, "agent");
;             xb_add(&bar[XB_XGEN(b.x)], 1u);
;             asm volatile("s_waitcnt vmcnt(0)" ::: "memory");
;         } else {
;             XB_SPIN(xb_ld(&bar[XB_XGEN(b.x)]) == gen, bar);
;             __builtin_amdgcn_fence(__ATOMIC_ACQUIRE, "agent");
;             asm volatile("s_waitcnt vmcnt(0)" ::: "memory");
;         }
;     }
;     __syncthreads();
; }
.LBB0_1375:
	s_cbranch_execnz .Lbw_ret_6
	s_mov_b32 s100, 6
	s_branch .Lbw_run

; __device__ __forceinline__ unsigned xb_ld(unsigned* p)              { return __hip_atomic_load(p, __ATOMIC_RELAXED, __HIP_MEMORY_SCOPE_AGENT); }
; __device__ __forceinline__ unsigned xb_add(unsigned* p, unsigned v) { return __hip_atomic_fetch_add(p, v, __ATOMIC_RELAXED, __HIP_MEMORY_SCOPE_AGENT); }
; #define XB_SPIN(cond, bar) do { unsigned _sp = 0; while (cond) { __builtin_amdgcn_s_sleep(1); \
;     if ((++_sp & 255u) == 0u) { if (xb_ld(&(bar)[XB_TMO])) break; if (_sp > XB_SPIN_CAP) { atomicAdd(&(bar)[XB_TMO], 1u); break; } } } } while (0)
; __device__ __forceinline__ void xcd_barrier(const XcdBarrier& b) {
;     asm volatile("s_waitcnt vmcnt(0)" ::: "memory");
;     __syncthreads();
;     if (threadIdx.x == 0) {
;         unsigned* bar = b.bar;
;         __builtin_amdgcn_s_waitcnt(0);
;         unsigned nloc = b.st[0], nx = b.st[1];
;         if (nloc == 0u) { xcd_barrier_complete(bar, b.x, nloc, nx); b.st[0] = nloc; b.st[1] = nx; }
;         const unsigned old = xb_add(&bar[XB_XSUB(b.x)], 1u);
;         const unsigned gen = old / nloc;
;         if (old + 1u == (gen + 1u) * nloc) {
;             __builtin_amdgcn_fence(__ATOMIC_RELEASE, "agent");
;             asm volatile("s_waitcnt vmcnt(0)" ::: "memory");
;             const unsigned og = xb_add(&bar[XB_TOP], 1u);
;             const unsigned tg = og / nx;
;             if (og + 1u == (tg + 1u) * nx) xb_add(&bar[XB_TOPGEN], 1u);
;             else XB_SPIN(xb_ld(&bar[XB_TOPGEN]) == tg, bar);
;             __builtin_amdgcn_fence(__ATOMIC_ACQUIRE, "agent");
;             xb_add(&bar[XB_XGEN(b.x)], 1u);
;             asm volatile("s_waitcnt vmcnt(0)" ::: "memory");
;         } else {
;             XB_SPIN(xb_ld(&bar[XB_XGEN(b.x)]) == gen, bar);
;             __builtin_amdgcn_fence(__ATOMIC_ACQUIRE, "agent");
;             asm volatile("s_waitcnt vmcnt(0)" ::: "memory");
;         }
;     }
;     __syncthreads();
; }
.LBB0_1452:
	s_cbranch_execnz .Lbw_ret_7
	s_mov_b32 s100, 7
	s_branch .Lbw_run

; __device__ __forceinline__ unsigned xb_ld(unsigned* p)              { return __hip_atomic_load(p, __ATOMIC_RELAXED, __HIP_MEMORY_SCOPE_AGENT); }
; __device__ __forceinline__ unsigned xb_add(unsigned* p, unsigned v) { return __hip_atomic_fetch_add(p, v, __ATOMIC_RELAXED, __HIP_MEMORY_SCOPE_AGENT); }
; #define XB_SPIN(cond, bar) do { unsigned _sp = 0; while (cond) { __builtin_amdgcn_s_sleep(1); \
;     if ((++_sp & 255u) == 0u) { if (xb_ld(&(bar)[XB_TMO])) break; if (_sp > XB_SPIN_CAP) { atomicAdd(&(bar)[XB_TMO], 1u); break; } } } } while (0)
; __device__ __forceinline__ void xcd_barrier(const XcdBarrier& b) {
;     asm volatile("s_waitcnt vmcnt(0)" ::: "memory");
;     __syncthreads();
;     if (threadIdx.x == 0) {
;         unsigned* bar = b.bar;
;         __builtin_amdgcn_s_waitcnt(0);
;         unsigned nloc = b.st[0], nx = b.st[1];
;         if (nloc == 0u) { xcd_barrier_complete(bar, b.x, nloc, nx); b.st[0] = nloc; b.st[1] = nx; }
;         const unsigned old = xb_add(&bar[XB_XSUB(b.x)], 1u);
;         const unsigned gen = old / nloc;
;         if (old + 1u == (gen + 1u) * nloc) {
;             __builtin_amdgcn_fence(__ATOMIC_RELEASE, "agent");
;             asm volatile("s_waitcnt vmcnt(0)" ::: "memory");
;             const unsigned og = xb_add(&bar[XB_TOP], 1u);
;             const unsigned tg = og / nx;
;             if (og + 1u == (tg + 1u) * nx) xb_add(&bar[XB_TOPGEN], 1u);
;             else XB_SPIN(xb_ld(&bar[XB_TOPGEN]) == tg, bar);
;             __builtin_amdgcn_fence(__ATOMIC_ACQUIRE, "agent");
;             xb_add(&bar[XB_XGEN(b.x)], 1u);
;             asm volatile("s_waitcnt vmcnt(0)" ::: "memory");
;         } else {
;             XB_SPIN(xb_ld(&bar[XB_XGEN(b.x)]) == gen, bar);
;             __builtin_amdgcn_fence(__ATOMIC_ACQUIRE, "agent");
;             asm volatile("s_waitcnt vmcnt(0)" ::: "memory");
;         }
;     }
;     __syncthreads();
; }
.LBB0_1547:
	s_cbranch_execnz .Lbw_ret_8
	s_mov_b32 s100, 8
	s_branch .Lbw_run

; __device__ __forceinline__ int moe_t1(int NT, int G) { const int t1 = NT < G / 4 ? NT : G / 4; return (4 * (NT - t1) < G / 2) ? t1 : NT; }
; #define INL(j) (((MK_PHMASK >> (j)) & 1) && INR(pb + (j)))
; #define SEAM(k) do { if (INR(k) && INR((k) + 1)) xcd_barrier(bar); F.lane = lane_id_v(); F.tid = F.wave * 64 + F.lane; { int z_; asm volatile("s_mov_b32 %0, 0" : "=s"(z_)); F.ws = args.ws + z_; F.out = args.out + z_; F.ctl = (gu32*)(args.ws + WS_CTL) + z_; F.in = args.in + z_; F.gw = gw0 + z_; } } while (0)
; __global__ void __launch_bounds__(NTHR, 2) mega_fwd(Args args) {
;     ...
; #pragma unroll 1
;         for (int sp = 0; sp < 3; ++sp) {
;             if (INL(10 + sp)) {
;                 if (sp == 0) moe_tables(F, l);
;                 const int NT = (int)F.MISC[MT_NT], T1 = moe_t1(NT, F.G), nUW = 4 * (NT - T1), nUR = (nUW + 7) & ~7;
;                 const bool doUp = sp == 0 || (sp == 1 && bx < nUW), doDown = (sp == 1 && bx >= nUR) || sp == 2;
;                 if (doUp) {
;                     SchedMoeUp Sc{F.MISC, (const char*)WSP(bf16_t, WS_W13 + l * SZ_W13), (char*)WSP(bf16_t, WS_HMID), WSP(int, WS_LIST), sp == 0 ? 0 : T1, sp == 0 ? 4 * T1 : nUW, bx, sp == 0 ? F.G : nUW};
;                     pg8::EpiSwiGLU E{WSP(float, WS_GATE), WSP(float, WS_RINV)};
;                     pg8::gemm_phase<pg8::EpiSwiGLU, SchedMoeUp, true, true>(F.wave, ring, D, D * 2, D * 2, (const char*)WSP(bf16_t, WS_XB), Sc, E);
;                 }
;                 if (doDown) {
;                     SchedMoeDown Sc{F.MISC, (const char*)WSP(bf16_t, WS_HMID), (const char*)WSP(bf16_t, WS_W2 + l * SZ_W2), (char*)WSP(bf16_t, WS_Y), sp == 1 ? 0 : T1, sp == 1 ? 8 * T1 : 8 * (NT - T1), sp == 1 ? bx - nUR : bx, sp == 1 ? F.G - nUR : F.G};
;                     pg8::EpiBf16 E{nullptr, 0};
;                     pg8::gemm_phase<pg8::EpiBf16, SchedMoeDown, false, false>(F.wave, ring, FH, FH * 2, FH * 2, nullptr, Sc, E);
;                 }
;             }
;             SEAM(pb + 10 + sp);
;         }
.LBB0_1552:
	v_readlane_b32 s100, v251, 3
	s_nop 3
	s_bitcmp1_b32 s100, 3
	s_cbranch_scc1 .Lcv_ret_9
	s_lshl_b32 s100, s87, 1
	s_add_i32 s100, s100, 8
	s_min_u32 s100, s100, 10
	s_cmp_ge_u32 s101, s100
	s_cbranch_scc1 .Lcv_ret_9
	s_lshl_b32 s100, s100, 8
	s_or_b32 s100, s100, 9
	s_branch .Lcv_run
.Lcv_ret_9:
	s_cmp_lg_u32 s101, 10
	s_cbranch_scc1 .Lcv_ret_10
	s_cmp_lg_u32 s87, 2
	s_cbranch_scc1 .Lcv_ret_10
	v_readlane_b32 s100, v251, 3
	s_nop 3
	s_bitcmp1_b32 s100, 3
	s_cbranch_scc1 .Lcv_ret_10
	s_bfe_u32 s100, s100, 0x50003
	s_cmp_lt_u32 s100, 30
	s_cbranch_scc1 .Lcv_ret_10
	s_mov_b32 s100, 50331658
	s_branch .Lcv_run

; __device__ __forceinline__ int moe_t1(int NT, int G) { const int t1 = NT < G / 4 ? NT : G / 4; return (4 * (NT - t1) < G / 2) ? t1 : NT; }
; #define INL(j) (((MK_PHMASK >> (j)) & 1) && INR(pb + (j)))
; #define SEAM(k) do { if (INR(k) && INR((k) + 1)) xcd_barrier(bar); F.lane = lane_id_v(); F.tid = F.wave * 64 + F.lane; { int z_; asm volatile("s_mov_b32 %0, 0" : "=s"(z_)); F.ws = args.ws + z_; F.out = args.out + z_; F.ctl = (gu32*)(args.ws + WS_CTL) + z_; F.in = args.in + z_; F.gw = gw0 + z_; } } while (0)
; __global__ void __launch_bounds__(NTHR, 2) mega_fwd(Args args) {
;     ...
; #pragma unroll 1
;         for (int sp = 0; sp < 3; ++sp) {
;             if (INL(10 + sp)) {
;                 if (sp == 0) moe_tables(F, l);
;                 const int NT = (int)F.MISC[MT_NT], T1 = moe_t1(NT, F.G), nUW = 4 * (NT - T1), nUR = (nUW + 7) & ~7;
;                 const bool doUp = sp == 0 || (sp == 1 && bx < nUW), doDown = (sp == 1 && bx >= nUR) || sp == 2;
;                 if (doUp) {
;                     SchedMoeUp Sc{F.MISC, (const char*)WSP(bf16_t, WS_W13 + l * SZ_W13), (char*)WSP(bf16_t, WS_HMID), WSP(int, WS_LIST), sp == 0 ? 0 : T1, sp == 0 ? 4 * T1 : nUW, bx, sp == 0 ? F.G : nUW};
;                     pg8::EpiSwiGLU E{WSP(float, WS_GATE), WSP(float, WS_RINV)};
;                     pg8::gemm_phase<pg8::EpiSwiGLU, SchedMoeUp, true, true>(F.wave, ring, D, D * 2, D * 2, (const char*)WSP(bf16_t, WS_XB), Sc, E);
;                 }
;                 if (doDown) {
;                     SchedMoeDown Sc{F.MISC, (const char*)WSP(bf16_t, WS_HMID), (const char*)WSP(bf16_t, WS_W2 + l * SZ_W2), (char*)WSP(bf16_t, WS_Y), sp == 1 ? 0 : T1, sp == 1 ? 8 * T1 : 8 * (NT - T1), sp == 1 ? bx - nUR : bx, sp == 1 ? F.G - nUR : F.G};
;                     pg8::EpiBf16 E{nullptr, 0};
;                     pg8::gemm_phase<pg8::EpiBf16, SchedMoeDown, false, false>(F.wave, ring, FH, FH * 2, FH * 2, nullptr, Sc, E);
;                 }
;             }
;             SEAM(pb + 10 + sp);
;         }
.LBB0_1642:
	s_add_i32 s94, s94, 1
	s_cmp_lt_i32 s94, s75
	s_cselect_b64 s[4:5], -1, 0
	s_and_b64 s[4:5], s[70:71], s[4:5]
	s_andn2_b64 vcc, exec, s[4:5]
	s_cbranch_vccnz .LBB0_1551
	v_readlane_b32 s100, v251, 3
	s_nop 3
	s_bitcmp1_b32 s100, 3
	s_cbranch_scc0 .Lcv_ret_11
	s_lshl_b32 s100, s87, 1
	s_add_i32 s100, s100, 8
	s_min_u32 s100, s100, 10
	s_cmp_ge_u32 s101, s100
	s_cbranch_scc1 .Lcv_ret_11
	s_lshl_b32 s100, s100, 8
	s_or_b32 s100, s100, 11
	s_branch .Lcv_run
.Lcv_ret_11:
	s_cmp_lg_u32 s101, 10
	s_cbranch_scc1 .Lcv_ret_12
	s_cmp_lg_u32 s87, 2
	s_cbranch_scc1 .Lcv_ret_12
	v_readlane_b32 s100, v251, 3
	s_nop 3
	s_bitcmp1_b32 s100, 3
	s_cbranch_scc0 .Lcv_ret_12
	s_bfe_u32 s100, s100, 0x50003
	s_cmp_lt_u32 s100, 30
	s_cbranch_scc1 .Lcv_ret_12
	s_mov_b32 s100, 50331660
	s_branch .Lcv_run
